# topk score tile: q tile and key blocks read with fully coalesced loads and staged through the free S area of LDS (xor swizzle) into the MFMA layout; same MFMAs and sum order
# baseline (speedup 1.0000x reference)
.LBB0_922:
	s_xor_b64 s[12:13], s[16:17], -1
	v_lshl_add_u64 v[80:81], s[14:15], 1, v[72:73]
	s_and_b64 s[14:15], s[16:17], exec
	s_mov_b32 s14, 0x100000
	s_cselect_b32 s84, s14, 0x180000
	v_lshl_add_u64 v[78:79], v[74:75], 0, s[84:85]
	s_mov_b32 s16, s7
	s_nop 1
	v_readfirstlane_b32 s18, v78
	v_readfirstlane_b32 s19, v79
	v_readfirstlane_b32 s100, v80
	v_readfirstlane_b32 s101, v81
	v_and_b32_e32 v251, 63, v0
	v_lshlrev_b32_e32 v248, 4, v251
	v_add_u32_e32 v249, 0x1000, v248
	v_and_b32_e32 v124, 15, v251
	v_lshrrev_b32_e32 v125, 4, v251
	v_lshlrev_b32_e32 v250, 4, v124
	v_lshl_add_u32 v250, v125, 12, v250
	v_xor_b32_e32 v126, v124, v125
	v_lshlrev_b32_e32 v126, 4, v126
	v_lshl_add_u32 v126, v125, 8, v126
	v_xor_b32_e32 v127, 0, v126
	v_add_u32_e32 v244, s5, v127
	v_xor_b32_e32 v127, 64, v126
	v_add_u32_e32 v245, s5, v127
	v_xor_b32_e32 v127, 128, v126
	v_add_u32_e32 v246, s5, v127
	v_xor_b32_e32 v127, 192, v126
	v_add_u32_e32 v247, s5, v127
	v_and_b32_e32 v124, 31, v251
	v_lshrrev_b32_e32 v125, 5, v251
	v_and_b32_e32 v126, 15, v124
	v_xor_b32_e32 v126, v126, v125
	v_lshlrev_b32_e32 v126, 4, v126
	v_lshl_add_u32 v126, v124, 8, v126
	v_add_u32_e32 v236, s5, v126
	v_xor_b32_e32 v127, 0x20, v126
	v_add_u32_e32 v237, s5, v127
	v_xor_b32_e32 v127, 0x40, v126
	v_add_u32_e32 v238, s5, v127
	v_xor_b32_e32 v127, 0x60, v126
	v_add_u32_e32 v239, s5, v127
	v_xor_b32_e32 v127, 0x80, v126
	v_add_u32_e32 v240, s5, v127
	v_xor_b32_e32 v127, 0xa0, v126
	v_add_u32_e32 v241, s5, v127
	v_xor_b32_e32 v127, 0xc0, v126
	v_add_u32_e32 v242, s5, v127
	v_xor_b32_e32 v127, 0xe0, v126
	v_add_u32_e32 v243, s5, v127
	global_load_dwordx4 v[116:119], v250, s[100:101] nt
	s_add_u32 s100, s100, 0x4000
	s_addc_u32 s101, s101, 0
	global_load_dwordx4 v[120:123], v250, s[100:101] nt
	s_add_u32 s100, s100, 0x4000
	s_addc_u32 s101, s101, 0
	global_load_dwordx4 v[130:133], v250, s[100:101] nt
	s_add_u32 s100, s100, 0x4000
	s_addc_u32 s101, s101, 0
	global_load_dwordx4 v[134:137], v250, s[100:101] nt
	s_add_u32 s100, s100, 0x4000
	s_addc_u32 s101, s101, 0
	global_load_dwordx4 v[138:141], v250, s[100:101] nt
	s_add_u32 s100, s100, 0x4000
	s_addc_u32 s101, s101, 0
	global_load_dwordx4 v[142:145], v250, s[100:101] nt
	s_add_u32 s100, s100, 0x4000
	s_addc_u32 s101, s101, 0
	global_load_dwordx4 v[146:149], v250, s[100:101] nt
	s_add_u32 s100, s100, 0x4000
	s_addc_u32 s101, s101, 0
	global_load_dwordx4 v[150:153], v250, s[100:101] nt
	global_load_dwordx4 v[154:157], v248, s[18:19]
	global_load_dwordx4 v[158:161], v248, s[18:19] offset:1024
	global_load_dwordx4 v[162:165], v248, s[18:19] offset:2048
	global_load_dwordx4 v[166:169], v248, s[18:19] offset:3072
	global_load_dwordx4 v[170:173], v249, s[18:19]
	global_load_dwordx4 v[176:179], v249, s[18:19] offset:1024
	global_load_dwordx4 v[180:183], v249, s[18:19] offset:2048
	global_load_dwordx4 v[184:187], v249, s[18:19] offset:3072
	s_add_u32 s18, s18, 0x2000
	s_addc_u32 s19, s19, 0
	global_load_dwordx4 v[188:191], v248, s[18:19]
	global_load_dwordx4 v[192:195], v248, s[18:19] offset:1024
	global_load_dwordx4 v[196:199], v248, s[18:19] offset:2048
	global_load_dwordx4 v[216:219], v248, s[18:19] offset:3072
	global_load_dwordx4 v[220:223], v249, s[18:19]
	global_load_dwordx4 v[224:227], v249, s[18:19] offset:1024
	global_load_dwordx4 v[228:231], v249, s[18:19] offset:2048
	global_load_dwordx4 v[232:235], v249, s[18:19] offset:3072
	s_add_u32 s18, s18, 0x2000
	s_addc_u32 s19, s19, 0
	global_load_dwordx4 v[22:25], v248, s[18:19]
	global_load_dwordx4 v[26:29], v248, s[18:19] offset:1024
	global_load_dwordx4 v[30:33], v248, s[18:19] offset:2048
	global_load_dwordx4 v[34:37], v248, s[18:19] offset:3072
	global_load_dwordx4 v[54:57], v249, s[18:19]
	global_load_dwordx4 v[58:61], v249, s[18:19] offset:1024
	global_load_dwordx4 v[62:65], v249, s[18:19] offset:2048
	global_load_dwordx4 v[66:69], v249, s[18:19] offset:3072
	s_add_u32 s18, s18, 0x2000
	s_addc_u32 s19, s19, 0
	s_waitcnt vmcnt(24)
	ds_write_b128 v244, v[116:119] offset:0
	ds_write_b128 v245, v[120:123] offset:1024
	ds_write_b128 v246, v[130:133] offset:2048
	ds_write_b128 v247, v[134:137] offset:3072
	ds_write_b128 v244, v[138:141] offset:4096
	ds_write_b128 v245, v[142:145] offset:5120
	ds_write_b128 v246, v[146:149] offset:6144
	ds_write_b128 v247, v[150:153] offset:7168
	s_waitcnt vmcnt(16)
	ds_write_b128 v244, v[154:157] offset:8192
	ds_write_b128 v245, v[158:161] offset:9216
	ds_write_b128 v246, v[162:165] offset:10240
	ds_write_b128 v247, v[166:169] offset:11264
	ds_write_b128 v244, v[170:173] offset:12288
	ds_write_b128 v245, v[176:179] offset:13312
	ds_write_b128 v246, v[180:183] offset:14336
	ds_write_b128 v247, v[184:187] offset:15360
	ds_read_b128 v[116:119], v236
	ds_read_b128 v[120:123], v237
	ds_read_b128 v[130:133], v238
	ds_read_b128 v[134:137], v239
	ds_read_b128 v[138:141], v240
	ds_read_b128 v[142:145], v241
	ds_read_b128 v[146:149], v242
	ds_read_b128 v[150:153], v243
	ds_read_b128 v[154:157], v236 offset:8192
	ds_read_b128 v[158:161], v237 offset:8192
	ds_read_b128 v[162:165], v238 offset:8192
	ds_read_b128 v[166:169], v239 offset:8192
	ds_read_b128 v[170:173], v240 offset:8192
	ds_read_b128 v[176:179], v241 offset:8192
	ds_read_b128 v[180:183], v242 offset:8192
	ds_read_b128 v[184:187], v243 offset:8192
	s_waitcnt lgkmcnt(0)
	v_mfma_f32_32x32x16_bf16 v[6:21], v[116:119], v[154:157], 0
	v_mfma_f32_32x32x16_bf16 v[6:21], v[120:123], v[158:161], v[6:21]
	v_mfma_f32_32x32x16_bf16 v[6:21], v[130:133], v[162:165], v[6:21]
	v_mfma_f32_32x32x16_bf16 v[6:21], v[134:137], v[166:169], v[6:21]
	v_mfma_f32_32x32x16_bf16 v[6:21], v[138:141], v[170:173], v[6:21]
	v_mfma_f32_32x32x16_bf16 v[6:21], v[142:145], v[176:179], v[6:21]
	v_mfma_f32_32x32x16_bf16 v[6:21], v[146:149], v[180:183], v[6:21]
	v_mfma_f32_32x32x16_bf16 v[6:21], v[150:153], v[184:187], v[6:21]
	global_load_dwordx4 v[154:157], v248, s[18:19]
	global_load_dwordx4 v[158:161], v248, s[18:19] offset:1024
	global_load_dwordx4 v[162:165], v248, s[18:19] offset:2048
	global_load_dwordx4 v[166:169], v248, s[18:19] offset:3072
	global_load_dwordx4 v[170:173], v249, s[18:19]
	global_load_dwordx4 v[176:179], v249, s[18:19] offset:1024
	global_load_dwordx4 v[180:183], v249, s[18:19] offset:2048
	global_load_dwordx4 v[184:187], v249, s[18:19] offset:3072
	s_waitcnt vmcnt(16)
	ds_write_b128 v244, v[188:191] offset:0
	ds_write_b128 v245, v[192:195] offset:1024
	ds_write_b128 v246, v[196:199] offset:2048
	ds_write_b128 v247, v[216:219] offset:3072
	ds_write_b128 v244, v[220:223] offset:4096
	ds_write_b128 v245, v[224:227] offset:5120
	ds_write_b128 v246, v[228:231] offset:6144
	ds_write_b128 v247, v[232:235] offset:7168
	ds_read_b128 v[188:191], v236
	ds_read_b128 v[192:195], v237
	ds_read_b128 v[196:199], v238
	ds_read_b128 v[216:219], v239
	ds_read_b128 v[220:223], v240
	ds_read_b128 v[224:227], v241
	ds_read_b128 v[228:231], v242
	ds_read_b128 v[232:235], v243
	s_waitcnt lgkmcnt(0)
	v_mfma_f32_32x32x16_bf16 v[38:53], v[116:119], v[188:191], 0
	v_mfma_f32_32x32x16_bf16 v[38:53], v[120:123], v[192:195], v[38:53]
	v_mfma_f32_32x32x16_bf16 v[38:53], v[130:133], v[196:199], v[38:53]
	v_mfma_f32_32x32x16_bf16 v[38:53], v[134:137], v[216:219], v[38:53]
	v_mfma_f32_32x32x16_bf16 v[38:53], v[138:141], v[220:223], v[38:53]
	v_mfma_f32_32x32x16_bf16 v[38:53], v[142:145], v[224:227], v[38:53]
	v_mfma_f32_32x32x16_bf16 v[38:53], v[146:149], v[228:231], v[38:53]
	v_mfma_f32_32x32x16_bf16 v[38:53], v[150:153], v[232:235], v[38:53]
	s_waitcnt vmcnt(8)
	ds_write_b128 v244, v[22:25] offset:8192
	ds_write_b128 v245, v[26:29] offset:9216
	ds_write_b128 v246, v[30:33] offset:10240
	ds_write_b128 v247, v[34:37] offset:11264
	ds_write_b128 v244, v[54:57] offset:12288
	ds_write_b128 v245, v[58:61] offset:13312
	ds_write_b128 v246, v[62:65] offset:14336
	ds_write_b128 v247, v[66:69] offset:15360
	ds_read_b128 v[188:191], v236 offset:8192
	ds_read_b128 v[192:195], v237 offset:8192
	ds_read_b128 v[196:199], v238 offset:8192
	ds_read_b128 v[216:219], v239 offset:8192
	ds_read_b128 v[220:223], v240 offset:8192
	ds_read_b128 v[224:227], v241 offset:8192
	ds_read_b128 v[228:231], v242 offset:8192
	ds_read_b128 v[232:235], v243 offset:8192
	s_waitcnt lgkmcnt(0)
	v_mfma_f32_32x32x16_bf16 v[22:37], v[116:119], v[188:191], 0
	v_mfma_f32_32x32x16_bf16 v[22:37], v[120:123], v[192:195], v[22:37]
	v_mfma_f32_32x32x16_bf16 v[22:37], v[130:133], v[196:199], v[22:37]
	v_mfma_f32_32x32x16_bf16 v[22:37], v[134:137], v[216:219], v[22:37]
	v_mfma_f32_32x32x16_bf16 v[22:37], v[138:141], v[220:223], v[22:37]
	v_mfma_f32_32x32x16_bf16 v[22:37], v[142:145], v[224:227], v[22:37]
	v_mfma_f32_32x32x16_bf16 v[22:37], v[146:149], v[228:231], v[22:37]
	v_mfma_f32_32x32x16_bf16 v[22:37], v[150:153], v[232:235], v[22:37]
	s_waitcnt vmcnt(0)
	ds_write_b128 v244, v[154:157] offset:0
	ds_write_b128 v245, v[158:161] offset:1024
	ds_write_b128 v246, v[162:165] offset:2048
	ds_write_b128 v247, v[166:169] offset:3072
	ds_write_b128 v244, v[170:173] offset:4096
	ds_write_b128 v245, v[176:179] offset:5120
	ds_write_b128 v246, v[180:183] offset:6144
	ds_write_b128 v247, v[184:187] offset:7168
	ds_read_b128 v[154:157], v236
	ds_read_b128 v[158:161], v237
	ds_read_b128 v[162:165], v238
	ds_read_b128 v[166:169], v239
	ds_read_b128 v[170:173], v240
	ds_read_b128 v[176:179], v241
	ds_read_b128 v[180:183], v242
	ds_read_b128 v[184:187], v243
	s_waitcnt lgkmcnt(0)
	v_mfma_f32_32x32x16_bf16 v[54:69], v[116:119], v[154:157], 0
	v_mfma_f32_32x32x16_bf16 v[54:69], v[120:123], v[158:161], v[54:69]
	v_mfma_f32_32x32x16_bf16 v[54:69], v[130:133], v[162:165], v[54:69]
	v_mfma_f32_32x32x16_bf16 v[54:69], v[134:137], v[166:169], v[54:69]
	v_mfma_f32_32x32x16_bf16 v[54:69], v[138:141], v[170:173], v[54:69]
	v_mfma_f32_32x32x16_bf16 v[54:69], v[142:145], v[176:179], v[54:69]
	v_mfma_f32_32x32x16_bf16 v[54:69], v[146:149], v[180:183], v[54:69]
	v_mfma_f32_32x32x16_bf16 v[54:69], v[150:153], v[184:187], v[54:69]
	s_nop 7
	ds_write2_b32 v93, v6, v38 offset1:32
	ds_write2_b32 v93, v7, v39 offset0:128 offset1:160
	v_add_u32_e32 v6, 0x400, v93
	ds_write2_b32 v6, v8, v40 offset1:32
	ds_write2_b32 v6, v9, v41 offset0:128 offset1:160
	v_add_u32_e32 v7, 0x1000, v93
	v_add_u32_e32 v8, 0x1400, v93
	ds_write2_b32 v7, v10, v42 offset1:32
	ds_write2_b32 v7, v11, v43 offset0:128 offset1:160
	ds_write2_b32 v8, v12, v44 offset1:32
	ds_write2_b32 v8, v13, v45 offset0:128 offset1:160
	v_add_u32_e32 v9, 0x2000, v93
	v_add_u32_e32 v10, 0x2400, v93
	v_add_u32_e32 v11, 0x3000, v93
	v_add_u32_e32 v12, 0x3400, v93
	ds_write2_b32 v9, v14, v46 offset1:32
	ds_write2_b32 v9, v15, v47 offset0:128 offset1:160
	ds_write2_b32 v10, v16, v48 offset1:32
	ds_write2_b32 v10, v17, v49 offset0:128 offset1:160
	ds_write2_b32 v11, v18, v50 offset1:32
	ds_write2_b32 v11, v19, v51 offset0:128 offset1:160
	v_mov_b32_e32 v13, v108
	v_mov_b32_e32 v14, v71
	ds_write2_b32 v12, v20, v52 offset1:32
	ds_write2_b32 v12, v21, v53 offset0:128 offset1:160
	s_nop 9
	ds_write2_b32 v93, v22, v54 offset0:64 offset1:96
	ds_write2_b32 v93, v23, v55 offset0:192 offset1:224
	ds_write2_b32 v6, v24, v56 offset0:64 offset1:96
	ds_write2_b32 v6, v25, v57 offset0:192 offset1:224
	ds_write2_b32 v7, v26, v58 offset0:64 offset1:96
	ds_write2_b32 v7, v27, v59 offset0:192 offset1:224
	ds_write2_b32 v8, v28, v60 offset0:64 offset1:96
	ds_write2_b32 v8, v29, v61 offset0:192 offset1:224
	ds_write2_b32 v9, v30, v62 offset0:64 offset1:96
	ds_write2_b32 v9, v31, v63 offset0:192 offset1:224
	ds_write2_b32 v10, v32, v64 offset0:64 offset1:96
	ds_write2_b32 v10, v33, v65 offset0:192 offset1:224
	ds_write2_b32 v11, v34, v66 offset0:64 offset1:96
	ds_write2_b32 v11, v35, v67 offset0:192 offset1:224
	ds_write2_b32 v12, v36, v68 offset0:64 offset1:96
	ds_write2_b32 v12, v37, v69 offset0:192 offset1:224
	s_andn2_b64 vcc, exec, s[10:11]
	s_waitcnt lgkmcnt(0)
	v_mov_b32_e32 v8, v114
	v_mov_b32_e32 v6, v113
	v_mov_b32_e32 v9, v112
	v_mov_b32_e32 v10, v111
	v_mov_b32_e32 v11, v110
	v_mov_b32_e32 v12, v109
	s_cbranch_vccz .LBB0_924
	s_branch .LBB0_921
